# MLA q up-projection: software-pipelined W-fragment LDS reads (ring of 6 quads, MFMAs deferred by 3)
# speedup vs baseline: 1.0151x; 1.0016x over previous
.LBB0_1224:
	v_mov_b32_e32 v0, v181
	v_readlane_b32 s8, v251, 6
	v_mbcnt_lo_u32_b32 v0, -1, v0
	v_mbcnt_hi_u32_b32 v203, -1, v0
	v_and_b32_e32 v205, 63, v203
	v_or_b32_e32 v0, s8, v205
	v_mul_hi_i32 v1, v0, s30
	v_lshrrev_b32_e32 v2, 31, v1
	v_ashrrev_i32_e32 v1, 2, v1
	v_add_u32_e32 v2, v1, v2
	v_mad_u64_u32 v[4:5], s[8:9], v2, s91, v[0:1]
	v_lshrrev_b32_e32 v1, 1, v2
	v_xor_b32_e32 v1, v1, v203
	v_bfi_b32 v1, -8, v4, v1
	v_cmp_lt_i32_e32 vcc, 15, v1
	v_ashrrev_i32_e32 v3, 31, v2
	v_lshlrev_b32_e32 v4, 3, v1
	s_and_saveexec_b64 s[8:9], vcc
	s_xor_b64 s[8:9], exec, s[8:9]
	v_lshlrev_b64 v[2:3], 7, v[2:3]
	v_lshl_add_u64 v[2:3], s[50:51], 0, v[2:3]
	v_add_u32_e32 v180, 0xffffff80, v4
	v_lshl_add_u64 v[16:17], v[180:181], 1, v[2:3]
	s_or_saveexec_b64 s[8:9], s[8:9]
	v_mov_b64_e32 v[18:19], 0x1000
	s_xor_b64 exec, exec, s[8:9]
	v_lshlrev_b64 v[2:3], 8, v[2:3]
	v_lshl_add_u64 v[2:3], s[48:49], 0, v[2:3]
	v_ashrrev_i32_e32 v5, 31, v4
	v_lshl_add_u64 v[16:17], v[4:5], 1, v[2:3]
	v_mov_b64_e32 v[18:19], 0x2000
	s_or_b64 exec, exec, s[8:9]
	v_add_u32_e32 v4, 0x200, v0
	v_mul_hi_i32 v1, v4, s30
	v_lshrrev_b32_e32 v2, 31, v1
	v_ashrrev_i32_e32 v1, 2, v1
	v_add_u32_e32 v2, v1, v2
	v_lshrrev_b32_e32 v1, 1, v2
	v_mad_u64_u32 v[4:5], s[8:9], v2, s91, v[4:5]
	v_xor_b32_e32 v1, v1, v203
	v_bfi_b32 v1, -8, v4, v1
	v_cmp_lt_i32_e32 vcc, 15, v1
	v_ashrrev_i32_e32 v3, 31, v2
	v_lshlrev_b32_e32 v4, 3, v1
	s_and_saveexec_b64 s[8:9], vcc
	s_xor_b64 s[8:9], exec, s[8:9]
	v_lshlrev_b64 v[2:3], 7, v[2:3]
	v_lshl_add_u64 v[2:3], s[50:51], 0, v[2:3]
	v_add_u32_e32 v180, 0xffffff80, v4
	v_lshl_add_u64 v[20:21], v[180:181], 1, v[2:3]
	s_or_saveexec_b64 s[8:9], s[8:9]
	v_mov_b64_e32 v[22:23], 0x1000
	s_xor_b64 exec, exec, s[8:9]
	v_lshlrev_b64 v[2:3], 8, v[2:3]
	v_lshl_add_u64 v[2:3], s[48:49], 0, v[2:3]
	v_ashrrev_i32_e32 v5, 31, v4
	v_lshl_add_u64 v[20:21], v[4:5], 1, v[2:3]
	v_mov_b64_e32 v[22:23], 0x2000
	s_or_b64 exec, exec, s[8:9]
	v_add_u32_e32 v2, 0x400, v0
	v_mul_hi_i32 v0, v2, s30
	v_lshrrev_b32_e32 v1, 31, v0
	v_ashrrev_i32_e32 v0, 2, v0
	v_add_u32_e32 v0, v0, v1
	v_lshrrev_b32_e32 v1, 1, v0
	v_mad_u64_u32 v[2:3], s[8:9], v0, s91, v[2:3]
	v_xor_b32_e32 v1, v1, v203
	v_bfi_b32 v2, -8, v2, v1
	v_cmp_lt_i32_e32 vcc, 15, v2
	v_ashrrev_i32_e32 v1, 31, v0
	v_lshlrev_b32_e32 v2, 3, v2
	s_and_saveexec_b64 s[8:9], vcc
	s_xor_b64 s[8:9], exec, s[8:9]
	v_lshlrev_b64 v[0:1], 7, v[0:1]
	v_lshl_add_u64 v[0:1], s[50:51], 0, v[0:1]
	v_add_u32_e32 v180, 0xffffff80, v2
	v_lshl_add_u64 v[24:25], v[180:181], 1, v[0:1]
	s_or_saveexec_b64 s[8:9], s[8:9]
	v_mov_b64_e32 v[26:27], 0x1000
	s_xor_b64 exec, exec, s[8:9]
	v_lshlrev_b64 v[0:1], 8, v[0:1]
	v_lshl_add_u64 v[0:1], s[48:49], 0, v[0:1]
	v_ashrrev_i32_e32 v3, 31, v2
	v_lshl_add_u64 v[24:25], v[2:3], 1, v[0:1]
	v_mov_b64_e32 v[26:27], 0x2000
	s_or_b64 exec, exec, s[8:9]
	s_xor_b64 s[58:59], s[4:5], -1
	s_xor_b64 s[60:61], s[6:7], -1
	s_and_b64 s[4:5], s[4:5], exec
	s_cselect_b32 s57, s79, s70
	s_lshl_b32 s21, s57, 8
	s_add_i32 s44, s21, s26
	s_add_u32 s66, s46, s44
	s_mov_b32 s4, s45
	s_mov_b32 s5, s45
	s_addc_u32 s67, s47, 0
	s_mov_b32 s6, s45
	s_mov_b32 s7, s45
	s_mov_b32 s8, s45
	s_mov_b32 s9, s45
	s_mov_b32 s10, s45
	s_mov_b32 s11, s45
	s_mov_b32 s12, s45
	s_mov_b32 s13, s45
	s_mov_b32 s14, s45
	s_mov_b32 s15, s45
	s_mov_b32 s16, s45
	s_mov_b32 s17, s45
	s_mov_b32 s18, s45
	s_mov_b32 s19, s45
	v_mov_b64_e32 v[0:1], s[4:5]
	v_mov_b64_e32 v[2:3], s[6:7]
	v_mov_b64_e32 v[4:5], s[8:9]
	v_mov_b64_e32 v[6:7], s[10:11]
	v_mov_b64_e32 v[8:9], s[12:13]
	v_mov_b64_e32 v[10:11], s[14:15]
	v_mov_b64_e32 v[12:13], s[16:17]
	v_mov_b64_e32 v[14:15], s[18:19]
	s_lshl_b64 s[4:5], s[66:67], 9
	v_readlane_b32 s6, v251, 38
	s_add_u32 s8, s6, s4
	v_readlane_b32 s4, v251, 39
	s_addc_u32 s9, s4, s5
	s_lshl_b64 s[4:5], s[66:67], 4
	v_readlane_b32 s6, v251, 43
	s_add_u32 s6, s6, s4
	v_readlane_b32 s4, v251, 45
	s_addc_u32 s7, s4, s5
	s_lshl_b64 s[4:5], s[44:45], 8
	v_readlane_b32 s10, v251, 47
	s_mov_b32 m0, s88
	s_add_u32 s4, s10, s4
	v_readlane_b32 s10, v251, 48
	s_addc_u32 s5, s10, s5
	global_load_lds_dwordx4 v[16:17], off
	v_lshlrev_b32_e32 v180, 1, v18
	s_add_i32 m0, s88, 0x2000
	v_lshrrev_b32_e32 v204, 5, v205
	v_readlane_b32 s10, v251, 63
	v_and_b32_e32 v200, 31, v203
	s_waitcnt vmcnt(0)
	v_lshl_add_u64 v[126:127], v[16:17], 0, v[180:181]
	global_load_lds_dwordx4 v[20:21], off
	s_mov_b32 m0, s86
	v_or_b32_e32 v16, s10, v204
	v_lshlrev_b32_e32 v184, 1, v22
	v_mov_b32_e32 v185, v181
	global_load_lds_dwordx4 v[24:25], off
	s_mov_b32 m0, s27
	v_bitop3_b32 v18, v16, v200, 9 bitop3:0x6c
	v_and_or_b32 v16, v16, 17, s96
	v_mov_b32_e32 v17, v181
	v_lshl_add_u64 v[188:189], v[20:21], 0, v[184:185]
	v_lshlrev_b32_e32 v186, 1, v26
	v_mov_b32_e32 v187, v181
	global_load_lds_dwordx4 v[126:127], off
	s_mov_b32 m0, s38
	v_lshlrev_b64 v[16:17], 9, v[16:17]
	v_lshl_add_u64 v[120:121], v[24:25], 0, v[186:187]
	global_load_lds_dwordx4 v[188:189], off
	s_mov_b32 m0, s39
	v_lshl_add_u64 v[16:17], s[34:35], 0, v[16:17]
	v_lshlrev_b32_e32 v18, 4, v18
	v_mov_b32_e32 v19, v181
	v_readlane_b32 s10, v250, 27
	global_load_lds_dwordx4 v[120:121], off
	v_lshl_add_u64 v[16:17], v[16:17], 0, v[18:19]
	s_mov_b32 m0, s10
	v_readlane_b32 s10, v251, 57
	global_load_lds_dwordx4 v[16:17], off
	s_nop 0
	v_or_b32_e32 v16, s10, v204
	v_bitop3_b32 v18, v16, v200, 11 bitop3:0x6c
	v_and_or_b32 v16, v16, 19, s96
	v_mov_b32_e32 v17, v181
	v_lshlrev_b64 v[16:17], 9, v[16:17]
	v_lshl_add_u64 v[16:17], s[34:35], 0, v[16:17]
	v_lshlrev_b32_e32 v18, 4, v18
	v_lshl_add_u64 v[16:17], v[16:17], 0, v[18:19]
	s_mov_b32 m0, s74
	v_readlane_b32 s10, v251, 61
	global_load_lds_dwordx4 v[16:17], off
	s_nop 0
	v_or_b32_e32 v16, s10, v204
	v_bitop3_b32 v18, v16, v200, 13 bitop3:0x6c
	v_and_or_b32 v16, v16, 17, s82
	v_mov_b32_e32 v17, v181
	v_lshlrev_b64 v[16:17], 9, v[16:17]
	v_lshl_add_u64 v[16:17], s[34:35], 0, v[16:17]
	v_lshlrev_b32_e32 v18, 4, v18
	v_lshl_add_u64 v[16:17], v[16:17], 0, v[18:19]
	s_mov_b32 m0, s76
	v_readlane_b32 s10, v250, 0
	global_load_lds_dwordx4 v[16:17], off
	s_nop 0
	v_or_b32_e32 v16, s10, v204
	v_bitop3_b32 v18, v16, v200, 15 bitop3:0x6c
	v_and_or_b32 v16, v16, 19, s82
	v_mov_b32_e32 v17, v181
	v_lshlrev_b64 v[16:17], 9, v[16:17]
	v_lshl_add_u64 v[16:17], s[34:35], 0, v[16:17]
	v_lshlrev_b32_e32 v18, 4, v18
	v_lshl_add_u64 v[16:17], v[16:17], 0, v[18:19]
	s_mov_b32 m0, s78
	v_readlane_b32 s10, v250, 6
	global_load_lds_dwordx4 v[16:17], off
	s_nop 0
	v_or_b32_e32 v16, s10, v204
	v_bitop3_b32 v18, v16, v200, 9 bitop3:0x6c
	v_and_or_b32 v16, v16, 17, s84
	v_mov_b32_e32 v17, v181
	v_lshlrev_b64 v[16:17], 9, v[16:17]
	v_lshl_add_u64 v[16:17], s[34:35], 0, v[16:17]
	v_lshlrev_b32_e32 v18, 4, v18
	v_lshl_add_u64 v[16:17], v[16:17], 0, v[18:19]
	s_mov_b32 m0, s94
	v_readlane_b32 s10, v250, 9
	global_load_lds_dwordx4 v[16:17], off
	s_nop 0
	v_or_b32_e32 v16, s10, v204
	v_bitop3_b32 v18, v16, v200, 11 bitop3:0x6c
	v_and_or_b32 v16, v16, 19, s36
	v_mov_b32_e32 v17, v181
	v_lshlrev_b64 v[16:17], 9, v[16:17]
	v_lshl_add_u64 v[16:17], s[34:35], 0, v[16:17]
	v_lshlrev_b32_e32 v18, 4, v18
	v_lshl_add_u64 v[16:17], v[16:17], 0, v[18:19]
	s_mov_b32 m0, s24
	v_lshlrev_b32_e32 v20, 9, v200
	global_load_lds_dwordx4 v[16:17], off
	v_or_b32_e32 v16, s73, v204
	v_bitop3_b32 v18, v16, v200, 13 bitop3:0x6c
	v_and_or_b32 v16, v16, 17, s37
	v_mov_b32_e32 v17, v181
	v_lshlrev_b64 v[16:17], 9, v[16:17]
	v_lshl_add_u64 v[16:17], s[34:35], 0, v[16:17]
	v_lshlrev_b32_e32 v18, 4, v18
	v_lshl_add_u64 v[16:17], v[16:17], 0, v[18:19]
	s_mov_b32 m0, s28
	v_mov_b32_e32 v21, v181
	global_load_lds_dwordx4 v[16:17], off
	v_or_b32_e32 v16, s72, v204
	v_bitop3_b32 v18, v16, v200, 15 bitop3:0x6c
	v_and_or_b32 v16, v16, 19, s85
	v_mov_b32_e32 v17, v181
	v_lshlrev_b64 v[16:17], 9, v[16:17]
	v_lshl_add_u64 v[16:17], s[34:35], 0, v[16:17]
	v_lshlrev_b32_e32 v18, 4, v18
	v_lshl_add_u64 v[16:17], v[16:17], 0, v[18:19]
	s_mov_b32 m0, s90
	v_lshlrev_b32_e32 v18, 8, v204
	global_load_lds_dwordx4 v[16:17], off
	v_or_b32_e32 v16, s97, v204
	v_bitop3_b32 v26, v16, v200, 9 bitop3:0x6c
	v_and_or_b32 v16, v16, 17, s83
	v_mov_b32_e32 v17, v181
	v_lshlrev_b64 v[22:23], 9, v[16:17]
	v_lshl_add_u64 v[16:17], s[8:9], 0, v[20:21]
	v_lshl_add_u64 v[24:25], v[16:17], 0, v[18:19]
	global_load_dwordx4 v[16:19], v[24:25], off
	global_load_dwordx4 v[172:175], v[24:25], off offset:16
	v_lshl_add_u64 v[22:23], s[34:35], 0, v[22:23]
	v_lshlrev_b32_e32 v26, 4, v26
	v_mov_b32_e32 v27, v181
	v_lshl_add_u64 v[22:23], v[22:23], 0, v[26:27]
	s_mov_b32 m0, s31
	v_or_b32_e32 v21, s41, v204
	global_load_lds_dwordx4 v[22:23], off
	v_and_or_b32 v22, v21, 19, s92
	v_mov_b32_e32 v23, v181
	v_bitop3_b32 v26, v21, v200, 11 bitop3:0x6c
	v_lshlrev_b64 v[22:23], 9, v[22:23]
	v_lshl_add_u64 v[22:23], s[34:35], 0, v[22:23]
	v_lshlrev_b32_e32 v26, 4, v26
	v_lshl_add_u64 v[22:23], v[22:23], 0, v[26:27]
	s_mov_b32 m0, s42
	v_or_b32_e32 v21, s75, v204
	global_load_lds_dwordx4 v[22:23], off
	v_and_or_b32 v22, v21, 17, s93
	v_mov_b32_e32 v23, v181
	v_bitop3_b32 v26, v21, v200, 13 bitop3:0x6c
	v_lshlrev_b64 v[22:23], 9, v[22:23]
	v_lshl_add_u64 v[22:23], s[34:35], 0, v[22:23]
	v_lshlrev_b32_e32 v26, 4, v26
	v_lshl_add_u64 v[22:23], v[22:23], 0, v[26:27]
	s_mov_b32 m0, s87
	v_or_b32_e32 v21, s77, v204
	global_load_lds_dwordx4 v[22:23], off
	v_and_or_b32 v22, v21, 19, s95
	v_mov_b32_e32 v23, v181
	v_bitop3_b32 v26, v21, v200, 15 bitop3:0x6c
	v_lshlrev_b64 v[22:23], 9, v[22:23]
	v_lshl_add_u64 v[22:23], s[34:35], 0, v[22:23]
	v_lshlrev_b32_e32 v26, 4, v26
	v_lshl_add_u64 v[22:23], v[22:23], 0, v[26:27]
	s_mov_b32 m0, s71
	v_lshlrev_b32_e32 v21, 4, v200
	global_load_lds_dwordx4 v[22:23], off
	global_load_dwordx4 v[168:171], v[24:25], off offset:32
	global_load_dwordx4 v[112:115], v[24:25], off offset:48
	global_load_dwordx4 v[116:119], v[24:25], off offset:64
	global_load_dwordx4 v[122:125], v[24:25], off offset:80
	global_load_dwordx4 v[164:167], v[24:25], off offset:96
	global_load_dwordx4 v[160:163], v[24:25], off offset:112
	global_load_dwordx4 v[156:159], v[24:25], off offset:128
	global_load_dwordx4 v[152:155], v[24:25], off offset:144
	global_load_dwordx4 v[148:151], v[24:25], off offset:160
	global_load_dwordx4 v[128:131], v[24:25], off offset:176
	global_load_dwordx4 v[144:147], v[24:25], off offset:192
	global_load_dwordx4 v[140:143], v[24:25], off offset:208
	global_load_dwordx4 v[132:135], v[24:25], off offset:224
	global_load_dwordx4 v[136:139], v[24:25], off offset:240
	v_lshlrev_b32_e32 v23, 4, v204
	v_and_b32_e32 v201, 15, v203
	global_load_dwordx4 v[176:179], v21, s[6:7]
	v_or_b32_e32 v21, v23, v201
	v_add_u32_e32 v22, 0, v20
	v_lshlrev_b32_e32 v21, 4, v21
	v_add_u32_e32 v228, v22, v21
	s_waitcnt vmcnt(0)
	s_waitcnt vmcnt(0) lgkmcnt(0)
	s_barrier
	ds_read_b128 v[228:231], v228 offset:49152
	v_add_u32_e32 v28, 0x10000, v22
	v_add_u32_e32 v232, v28, v21
	ds_read_b128 v[232:235], v232
	v_add_u32_e32 v221, s43, v20
	v_add_u32_e32 v218, 0x20400, v22
	v_readlane_b32 s6, v251, 6
	s_lshl_b32 s9, s57, 2
	s_add_i32 s9, s9, 4
	v_bitop3_b32 v24, v23, v201, 1 bitop3:0x36
	v_lshlrev_b32_e32 v202, 4, v24
	v_add_u32_e32 v236, v22, v202
	ds_read_b128 v[236:239], v236 offset:49152
	v_add_u32_e32 v222, v221, v202
	s_ashr_i32 s11, s89, 31
	s_mov_b32 s10, 3
	v_add_u32_e32 v240, v28, v202
	ds_read_b128 v[240:243], v240
	ds_read_b128 v[222:225], v222
	s_waitcnt lgkmcnt(4)
	v_mfma_f32_32x32x16_bf16 v[64:79], v[228:231], v[16:19], 0
	v_bitop3_b32 v24, v23, v201, 2 bitop3:0x36
	v_lshlrev_b32_e32 v220, 4, v24
	v_add_u32_e32 v244, v22, v220
	ds_read_b128 v[244:247], v244 offset:49152
	s_waitcnt lgkmcnt(4)
	v_mfma_f32_32x32x16_bf16 v[48:63], v[232:235], v[16:19], 0
	v_add_u32_e32 v252, v28, v220
	ds_read_b128 v[252:255], v252
	s_waitcnt lgkmcnt(4)
	v_mfma_f32_32x32x16_bf16 v[64:79], v[236:239], v[172:175], v[64:79]
	v_bitop3_b32 v24, v23, v201, 3 bitop3:0x36
	v_lshlrev_b32_e32 v219, 4, v24
	v_add_u32_e32 v228, v22, v219
	ds_read_b128 v[228:231], v228 offset:49152
	s_waitcnt lgkmcnt(4)
	v_mfma_f32_32x32x16_bf16 v[48:63], v[240:243], v[172:175], v[48:63]
	v_add_u32_e32 v232, v28, v219
	ds_read_b128 v[232:235], v232
	s_waitcnt lgkmcnt(3)
	v_mfma_f32_32x32x16_bf16 v[64:79], v[244:247], v[168:171], v[64:79]
	v_bitop3_b32 v24, v23, v201, 4 bitop3:0x36
	v_lshlrev_b32_e32 v217, 4, v24
	v_add_u32_e32 v236, v22, v217
	ds_read_b128 v[236:239], v236 offset:49152
	s_waitcnt lgkmcnt(3)
	v_mfma_f32_32x32x16_bf16 v[48:63], v[252:255], v[168:171], v[48:63]
	v_add_u32_e32 v240, v28, v217
	ds_read_b128 v[240:243], v240
	s_waitcnt lgkmcnt(3)
	v_mfma_f32_32x32x16_bf16 v[64:79], v[228:231], v[112:115], v[64:79]
	v_bitop3_b32 v24, v23, v201, 5 bitop3:0x36
	v_lshlrev_b32_e32 v216, 4, v24
	v_add_u32_e32 v244, v22, v216
	ds_read_b128 v[244:247], v244 offset:49152
	s_waitcnt lgkmcnt(3)
	v_mfma_f32_32x32x16_bf16 v[48:63], v[232:235], v[112:115], v[48:63]
	v_add_u32_e32 v252, v28, v216
	ds_read_b128 v[252:255], v252
	s_waitcnt lgkmcnt(3)
	v_mfma_f32_32x32x16_bf16 v[64:79], v[236:239], v[116:119], v[64:79]
	v_bitop3_b32 v24, v23, v201, 6 bitop3:0x36
	v_lshlrev_b32_e32 v215, 4, v24
	v_add_u32_e32 v228, v22, v215
	ds_read_b128 v[228:231], v228 offset:49152
	s_waitcnt lgkmcnt(3)
	v_mfma_f32_32x32x16_bf16 v[48:63], v[240:243], v[116:119], v[48:63]
	v_add_u32_e32 v232, v28, v215
	ds_read_b128 v[232:235], v232
	s_waitcnt lgkmcnt(3)
	v_mfma_f32_32x32x16_bf16 v[64:79], v[244:247], v[122:125], v[64:79]
	v_bitop3_b32 v24, v23, v201, 7 bitop3:0x36
	v_lshlrev_b32_e32 v214, 4, v24
	v_add_u32_e32 v236, v22, v214
	ds_read_b128 v[236:239], v236 offset:49152
	s_waitcnt lgkmcnt(3)
	v_mfma_f32_32x32x16_bf16 v[48:63], v[252:255], v[122:125], v[48:63]
	v_add_u32_e32 v240, v28, v214
	ds_read_b128 v[240:243], v240
	s_waitcnt lgkmcnt(3)
	v_mfma_f32_32x32x16_bf16 v[64:79], v[228:231], v[164:167], v[64:79]
	v_bitop3_b32 v24, v23, v201, 8 bitop3:0x36
	v_lshlrev_b32_e32 v210, 4, v24
	v_add_u32_e32 v244, v22, v210
	ds_read_b128 v[244:247], v244 offset:49152
	s_waitcnt lgkmcnt(3)
	v_mfma_f32_32x32x16_bf16 v[48:63], v[232:235], v[164:167], v[48:63]
	v_add_u32_e32 v252, v28, v210
	ds_read_b128 v[252:255], v252
	s_waitcnt lgkmcnt(3)
	v_mfma_f32_32x32x16_bf16 v[64:79], v[236:239], v[160:163], v[64:79]
	v_bitop3_b32 v24, v23, v201, 9 bitop3:0x36
	v_lshlrev_b32_e32 v211, 4, v24
	v_add_u32_e32 v228, v22, v211
	ds_read_b128 v[228:231], v228 offset:49152
	s_waitcnt lgkmcnt(3)
	v_mfma_f32_32x32x16_bf16 v[48:63], v[240:243], v[160:163], v[48:63]
	v_add_u32_e32 v232, v28, v211
	ds_read_b128 v[232:235], v232
	s_waitcnt lgkmcnt(3)
	v_mfma_f32_32x32x16_bf16 v[64:79], v[244:247], v[156:159], v[64:79]
	v_bitop3_b32 v24, v23, v201, 10 bitop3:0x36
	v_lshlrev_b32_e32 v212, 4, v24
	v_add_u32_e32 v236, v22, v212
	ds_read_b128 v[236:239], v236 offset:49152
	s_waitcnt lgkmcnt(3)
	v_mfma_f32_32x32x16_bf16 v[48:63], v[252:255], v[156:159], v[48:63]
	v_add_u32_e32 v240, v28, v212
	ds_read_b128 v[240:243], v240
	s_waitcnt lgkmcnt(3)
	v_mfma_f32_32x32x16_bf16 v[64:79], v[228:231], v[152:155], v[64:79]
	v_bitop3_b32 v24, v23, v201, 11 bitop3:0x36
	v_lshlrev_b32_e32 v213, 4, v24
	v_add_u32_e32 v244, v22, v213
	ds_read_b128 v[244:247], v244 offset:49152
	s_waitcnt lgkmcnt(3)
	v_mfma_f32_32x32x16_bf16 v[48:63], v[232:235], v[152:155], v[48:63]
	v_add_u32_e32 v252, v28, v213
	ds_read_b128 v[252:255], v252
	s_waitcnt lgkmcnt(3)
	v_mfma_f32_32x32x16_bf16 v[64:79], v[236:239], v[148:151], v[64:79]
	v_bitop3_b32 v24, v23, v201, 12 bitop3:0x36
	v_lshlrev_b32_e32 v206, 4, v24
	v_add_u32_e32 v228, v22, v206
	ds_read_b128 v[228:231], v228 offset:49152
	s_waitcnt lgkmcnt(3)
	v_mfma_f32_32x32x16_bf16 v[48:63], v[240:243], v[148:151], v[48:63]
	v_add_u32_e32 v232, v28, v206
	ds_read_b128 v[232:235], v232
	s_waitcnt lgkmcnt(3)
	v_mfma_f32_32x32x16_bf16 v[64:79], v[244:247], v[128:131], v[64:79]
	v_bitop3_b32 v24, v23, v201, 13 bitop3:0x36
	v_lshlrev_b32_e32 v207, 4, v24
	v_add_u32_e32 v236, v22, v207
	ds_read_b128 v[236:239], v236 offset:49152
	s_waitcnt lgkmcnt(3)
	v_mfma_f32_32x32x16_bf16 v[48:63], v[252:255], v[128:131], v[48:63]
	v_add_u32_e32 v240, v28, v207
	ds_read_b128 v[240:243], v240
	s_waitcnt lgkmcnt(3)
	v_mfma_f32_32x32x16_bf16 v[64:79], v[228:231], v[144:147], v[64:79]
	v_bitop3_b32 v24, v23, v201, 14 bitop3:0x36
	v_lshlrev_b32_e32 v208, 4, v24
	v_add_u32_e32 v244, v22, v208
	ds_read_b128 v[244:247], v244 offset:49152
	v_bitop3_b32 v23, v23, v203, 15 bitop3:0x72
	v_lshlrev_b32_e32 v209, 4, v23
	v_add_u32_e32 v23, v22, v209
	s_waitcnt lgkmcnt(3)
	v_mfma_f32_32x32x16_bf16 v[48:63], v[232:235], v[144:147], v[48:63]
	v_add_u32_e32 v252, v28, v208
	ds_read_b128 v[252:255], v252
	s_waitcnt lgkmcnt(3)
	v_mfma_f32_32x32x16_bf16 v[64:79], v[236:239], v[140:143], v[64:79]
	ds_read_b128 v[228:231], v23 offset:49152
	v_add_u32_e32 v23, v28, v209
	v_add_u32_e32 v28, 0x18000, v22
	v_add_u32_e32 v29, v28, v213
	s_waitcnt lgkmcnt(3)
	v_mfma_f32_32x32x16_bf16 v[48:63], v[240:243], v[140:143], v[48:63]
	ds_read_b128 v[232:235], v23
	v_add_u32_e32 v23, s33, v20
	v_add_u32_e32 v20, v221, v21
	s_waitcnt lgkmcnt(3)
	v_mfma_f32_32x32x16_bf16 v[64:79], v[244:247], v[132:135], v[64:79]
	s_waitcnt lgkmcnt(2)
	v_mfma_f32_32x32x16_bf16 v[48:63], v[252:255], v[132:135], v[48:63]
	s_waitcnt lgkmcnt(1)
	v_mfma_f32_32x32x16_bf16 v[64:79], v[228:231], v[136:139], v[64:79]
	s_waitcnt lgkmcnt(0)
	v_mfma_f32_32x32x16_bf16 v[48:63], v[232:235], v[136:139], v[48:63]
	v_add_u32_e32 v236, v23, v21
	ds_read_b128 v[236:239], v236
	v_add_u32_e32 v240, v28, v21
	ds_read_b128 v[240:243], v240
	v_add_u32_e32 v244, v23, v202
	ds_read_b128 v[244:247], v244
	v_add_u32_e32 v252, v28, v202
	ds_read_b128 v[252:255], v252
	v_add_u32_e32 v202, v218, v202
	s_waitcnt lgkmcnt(3)
	v_mfma_f32_32x32x16_bf16 v[96:111], v[236:239], v[16:19], 0
	v_add_u32_e32 v228, v23, v220
	ds_read_b128 v[228:231], v228
	s_waitcnt lgkmcnt(3)
	v_mfma_f32_32x32x16_bf16 v[80:95], v[240:243], v[16:19], 0
	v_add_u32_e32 v232, v28, v220
	ds_read_b128 v[232:235], v232
	s_waitcnt lgkmcnt(3)
	v_mfma_f32_32x32x16_bf16 v[96:111], v[244:247], v[172:175], v[96:111]
	v_add_u32_e32 v236, v23, v219
	ds_read_b128 v[236:239], v236
	s_waitcnt lgkmcnt(3)
	v_mfma_f32_32x32x16_bf16 v[80:95], v[252:255], v[172:175], v[80:95]
	v_add_u32_e32 v240, v28, v219
	ds_read_b128 v[240:243], v240
	s_waitcnt lgkmcnt(3)
	v_mfma_f32_32x32x16_bf16 v[96:111], v[228:231], v[168:171], v[96:111]
	v_add_u32_e32 v244, v23, v217
	ds_read_b128 v[244:247], v244
	s_waitcnt lgkmcnt(3)
	v_mfma_f32_32x32x16_bf16 v[80:95], v[232:235], v[168:171], v[80:95]
	v_add_u32_e32 v252, v28, v217
	ds_read_b128 v[252:255], v252
	s_waitcnt lgkmcnt(3)
	v_mfma_f32_32x32x16_bf16 v[96:111], v[236:239], v[112:115], v[96:111]
	v_add_u32_e32 v228, v23, v216
	ds_read_b128 v[228:231], v228
	s_waitcnt lgkmcnt(3)
	v_mfma_f32_32x32x16_bf16 v[80:95], v[240:243], v[112:115], v[80:95]
	v_add_u32_e32 v232, v28, v216
	ds_read_b128 v[232:235], v232
	s_waitcnt lgkmcnt(3)
	v_mfma_f32_32x32x16_bf16 v[96:111], v[244:247], v[116:119], v[96:111]
	v_add_u32_e32 v236, v23, v215
	ds_read_b128 v[236:239], v236
	s_waitcnt lgkmcnt(3)
	v_mfma_f32_32x32x16_bf16 v[80:95], v[252:255], v[116:119], v[80:95]
	v_add_u32_e32 v240, v28, v215
	ds_read_b128 v[240:243], v240
	s_waitcnt lgkmcnt(3)
	v_mfma_f32_32x32x16_bf16 v[96:111], v[228:231], v[122:125], v[96:111]
	v_add_u32_e32 v244, v23, v214
	ds_read_b128 v[244:247], v244
	s_waitcnt lgkmcnt(3)
	v_mfma_f32_32x32x16_bf16 v[80:95], v[232:235], v[122:125], v[80:95]
	v_add_u32_e32 v252, v28, v214
	ds_read_b128 v[252:255], v252
	s_waitcnt lgkmcnt(3)
	v_mfma_f32_32x32x16_bf16 v[96:111], v[236:239], v[164:167], v[96:111]
	v_add_u32_e32 v228, v23, v210
	ds_read_b128 v[228:231], v228
	s_waitcnt lgkmcnt(3)
	v_mfma_f32_32x32x16_bf16 v[80:95], v[240:243], v[164:167], v[80:95]
	v_add_u32_e32 v232, v28, v210
	ds_read_b128 v[232:235], v232
	s_waitcnt lgkmcnt(3)
	v_mfma_f32_32x32x16_bf16 v[96:111], v[244:247], v[160:163], v[96:111]
	v_add_u32_e32 v236, v23, v211
	ds_read_b128 v[236:239], v236
	s_waitcnt lgkmcnt(3)
	v_mfma_f32_32x32x16_bf16 v[80:95], v[252:255], v[160:163], v[80:95]
	v_add_u32_e32 v240, v28, v211
	ds_read_b128 v[240:243], v240
	s_waitcnt lgkmcnt(3)
	v_mfma_f32_32x32x16_bf16 v[96:111], v[228:231], v[156:159], v[96:111]
	v_add_u32_e32 v244, v23, v212
	ds_read_b128 v[244:247], v244
	s_waitcnt lgkmcnt(3)
	v_mfma_f32_32x32x16_bf16 v[80:95], v[232:235], v[156:159], v[80:95]
	v_add_u32_e32 v252, v28, v212
	ds_read_b128 v[252:255], v252
	s_waitcnt lgkmcnt(3)
	v_mfma_f32_32x32x16_bf16 v[96:111], v[236:239], v[152:155], v[96:111]
	v_add_u32_e32 v228, v23, v213
	ds_read_b128 v[228:231], v228
	s_waitcnt lgkmcnt(3)
	v_mfma_f32_32x32x16_bf16 v[80:95], v[240:243], v[152:155], v[80:95]
	ds_read_b128 v[232:235], v29
	v_add_u32_e32 v29, v23, v206
	s_waitcnt lgkmcnt(3)
	v_mfma_f32_32x32x16_bf16 v[96:111], v[244:247], v[148:151], v[96:111]
	ds_read_b128 v[236:239], v29
	v_add_u32_e32 v29, v28, v206
	s_waitcnt lgkmcnt(3)
	v_mfma_f32_32x32x16_bf16 v[80:95], v[252:255], v[148:151], v[80:95]
	ds_read_b128 v[240:243], v29
	v_add_u32_e32 v29, v23, v207
	s_waitcnt lgkmcnt(3)
	v_mfma_f32_32x32x16_bf16 v[96:111], v[228:231], v[128:131], v[96:111]
	ds_read_b128 v[244:247], v29
	v_add_u32_e32 v29, v28, v207
	s_waitcnt lgkmcnt(3)
	v_mfma_f32_32x32x16_bf16 v[80:95], v[232:235], v[128:131], v[80:95]
	ds_read_b128 v[252:255], v29
	v_add_u32_e32 v29, v23, v208
	v_add_u32_e32 v23, v23, v209
	s_waitcnt lgkmcnt(3)
	v_mfma_f32_32x32x16_bf16 v[96:111], v[236:239], v[144:147], v[96:111]
	ds_read_b128 v[228:231], v29
	v_add_u32_e32 v29, v28, v208
	s_waitcnt lgkmcnt(3)
	v_mfma_f32_32x32x16_bf16 v[80:95], v[240:243], v[144:147], v[80:95]
	ds_read_b128 v[232:235], v29
	s_waitcnt lgkmcnt(3)
	v_mfma_f32_32x32x16_bf16 v[96:111], v[244:247], v[140:143], v[96:111]
	ds_read_b128 v[236:239], v23
	v_add_u32_e32 v23, v28, v209
	s_waitcnt lgkmcnt(3)
	v_mfma_f32_32x32x16_bf16 v[80:95], v[252:255], v[140:143], v[80:95]
	ds_read_b128 v[240:243], v23
	s_waitcnt lgkmcnt(3)
	v_mfma_f32_32x32x16_bf16 v[96:111], v[228:231], v[132:135], v[96:111]
	s_waitcnt lgkmcnt(2)
	v_mfma_f32_32x32x16_bf16 v[80:95], v[232:235], v[132:135], v[80:95]
	s_waitcnt lgkmcnt(1)
	v_mfma_f32_32x32x16_bf16 v[96:111], v[236:239], v[136:139], v[96:111]
	s_waitcnt lgkmcnt(0)
	v_mfma_f32_32x32x16_bf16 v[80:95], v[240:243], v[136:139], v[80:95]
	ds_read_b128 v[24:27], v20
	v_add_u32_e32 v20, v218, v21
	ds_read_b128 v[20:23], v20
	s_waitcnt lgkmcnt(1)
	v_mfma_f32_32x32x16_bf16 v[32:47], v[24:27], v[16:19], 0
	v_mfma_f32_32x32x16_bf16 v[32:47], v[222:225], v[172:175], v[32:47]
	ds_read_b128 v[222:225], v202
	v_add_u32_e32 v202, v221, v220
	ds_read_b128 v[226:229], v202
	s_waitcnt lgkmcnt(2)
	v_mfma_f32_32x32x16_bf16 v[16:31], v[20:23], v[16:19], 0
	s_waitcnt lgkmcnt(1)
	v_mfma_f32_32x32x16_bf16 v[16:31], v[222:225], v[172:175], v[16:31]
	v_lshl_add_u64 v[174:175], v[126:127], 0, v[180:181]
	v_add_u32_e32 v126, v218, v220
	ds_read_b128 v[222:225], v126
	v_mov_b32_e32 v126, v177
	v_add_u32_e32 v177, v221, v219
	v_mov_b32_e32 v127, v178
	v_lshl_add_u64 v[172:173], v[188:189], 0, v[184:185]
	s_waitcnt lgkmcnt(1)
	v_mfma_f32_32x32x16_bf16 v[32:47], v[226:229], v[168:171], v[32:47]
	ds_read_b128 v[226:229], v177
	v_mov_b32_e32 v177, v179
	v_add_f32_e64 v126, v126, v176
	v_add_f32_e64 v127, v127, v177
	v_lshl_add_u64 v[188:189], v[120:121], 0, v[186:187]
	v_add_f32_e32 v126, v126, v127
	v_add_u32_e32 v127, v218, v219
	ds_read_b128 v[176:179], v127
	s_waitcnt lgkmcnt(2)
	v_mfma_f32_32x32x16_bf16 v[16:31], v[222:225], v[168:171], v[16:31]
	v_fmamk_f32 v126, v126, 0x3b800000, v198
	v_rsq_f32_e32 v126, v126
	v_lshlrev_b32_e32 v120, 8, v200
	v_mov_b32_e32 v121, v181
	v_lshl_add_u64 v[170:171], s[4:5], 0, v[120:121]
	v_mul_f32_e32 v168, 0x3dd53b94, v126
	v_lshlrev_b32_e32 v169, 3, v204
	v_add_u32_e32 v120, v221, v217
	ds_read_b128 v[222:225], v120
	v_pk_mul_f32 v[64:65], v[168:169], v[64:65] op_sel_hi:[0,1]
	s_waitcnt lgkmcnt(2)
	v_mfma_f32_32x32x16_bf16 v[32:47], v[226:229], v[112:115], v[32:47]
	v_mul_f32_e64 v66, v168, v66
	v_mul_f32_e64 v67, v168, v67
	v_mul_f32_e64 v68, v168, v68
	v_mul_f32_e64 v69, v168, v69
	v_mul_f32_e64 v70, v168, v70
	v_mul_f32_e64 v71, v168, v71
	v_pk_mul_f32 v[48:49], v[168:169], v[48:49] op_sel_hi:[0,1]
	v_cvt_pk_bf16_f32 v120, v48, v49
	v_add_u32_e32 v48, v221, v215
	v_pk_mul_f32 v[78:79], v[168:169], v[78:79] op_sel_hi:[0,1]
	s_waitcnt lgkmcnt(1)
	v_mfma_f32_32x32x16_bf16 v[16:31], v[176:179], v[112:115], v[16:31]
	v_cvt_pk_bf16_f32 v112, v64, v65
	v_add_u32_e32 v64, v218, v217
	v_cvt_pk_bf16_f32 v113, v66, v67
	ds_read_b128 v[64:67], v64
	v_cvt_pk_bf16_f32 v114, v68, v69
	v_add_u32_e32 v68, v221, v216
	v_cvt_pk_bf16_f32 v115, v70, v71
	ds_read_b128 v[68:71], v68
	s_waitcnt lgkmcnt(2)
	v_mfma_f32_32x32x16_bf16 v[32:47], v[222:225], v[116:119], v[32:47]
	v_mul_f32_e64 v52, v168, v52
	v_mul_f32_e64 v53, v168, v53
	v_mul_f32_e64 v54, v168, v54
	v_mul_f32_e64 v55, v168, v55
	v_mul_f32_e64 v72, v168, v72
	v_mul_f32_e64 v73, v168, v73
	v_pk_mul_f32 v[60:61], v[168:169], v[60:61] op_sel_hi:[0,1]
	v_pk_mul_f32 v[62:63], v[168:169], v[62:63] op_sel_hi:[0,1]
	v_cvt_pk_bf16_f32 v126, v60, v61
	v_cvt_pk_bf16_f32 v127, v62, v63
	s_waitcnt lgkmcnt(1)
	v_mfma_f32_32x32x16_bf16 v[16:31], v[64:67], v[116:119], v[16:31]
	v_mul_f32_e64 v64, v168, v74
	v_mul_f32_e64 v65, v168, v75
	v_cvt_pk_bf16_f32 v117, v64, v65
	v_add_u32_e32 v64, v218, v216
	ds_read_b128 v[64:67], v64
	v_cvt_pk_bf16_f32 v119, v78, v79
	v_pk_mul_f32 v[78:79], v[168:169], v[88:89] op_sel_hi:[0,1]
	v_cvt_pk_bf16_f32 v116, v72, v73
	s_waitcnt lgkmcnt(1)
	v_mfma_f32_32x32x16_bf16 v[32:47], v[68:71], v[122:125], v[32:47]
	v_mul_f32_e64 v68, v168, v50
	v_mul_f32_e64 v69, v168, v51
	ds_read_b128 v[48:51], v48
	v_mul_f32_e64 v70, v168, v86
	v_mul_f32_e64 v71, v168, v87
	v_add_u32_e32 v86, v218, v213
	ds_read_b128 v[86:89], v86
	v_pk_mul_f32 v[60:61], v[168:169], v[100:101] op_sel_hi:[0,1]
	v_pk_mul_f32 v[62:63], v[168:169], v[102:103] op_sel_hi:[0,1]
	s_waitcnt lgkmcnt(2)
	v_mfma_f32_32x32x16_bf16 v[16:31], v[64:67], v[122:125], v[16:31]
	v_cvt_pk_bf16_f32 v122, v52, v53
	v_add_u32_e32 v52, v218, v215
	v_cvt_pk_bf16_f32 v123, v54, v55
	ds_read_b128 v[52:55], v52
	v_mul_f32_e64 v64, v168, v98
	v_mul_f32_e64 v65, v168, v99
	v_cvt_pk_bf16_f32 v98, v60, v61
	v_cvt_pk_bf16_f32 v99, v62, v63
	s_waitcnt lgkmcnt(2)
	v_mfma_f32_32x32x16_bf16 v[32:47], v[48:51], v[164:167], v[32:47]
	v_mul_f32_e64 v48, v168, v56
	v_mul_f32_e64 v49, v168, v57
	v_mul_f32_e64 v50, v168, v58
	v_mul_f32_e64 v51, v168, v59
	v_cvt_pk_bf16_f32 v124, v48, v49
	v_add_u32_e32 v48, v221, v214
	v_cvt_pk_bf16_f32 v125, v50, v51
	ds_read_b128 v[48:51], v48
	v_and_b32_e32 v58, 32, v205
	s_waitcnt lgkmcnt(1)
	v_mfma_f32_32x32x16_bf16 v[16:31], v[52:55], v[164:167], v[16:31]
	v_add_u32_e32 v52, v218, v214
	ds_read_b128 v[52:55], v52
	v_mov_b32_e32 v59, v181
	v_lshl_add_u64 v[72:73], v[170:171], 0, v[58:59]
	v_mul_f32_e64 v56, v168, v96
	v_mul_f32_e64 v57, v168, v97
	v_cvt_pk_bf16_f32 v96, v56, v57
	v_add_u32_e32 v56, v221, v210
	s_waitcnt lgkmcnt(1)
	v_mfma_f32_32x32x16_bf16 v[32:47], v[48:51], v[160:163], v[32:47]
	global_load_dwordx4 v[48:51], v[72:73], off offset:16
	ds_read_b128 v[56:59], v56
	v_cvt_pk_bf16_f32 v97, v64, v65
	v_mul_f32_e64 v64, v168, v106
	v_mul_f32_e64 v65, v168, v107
	v_cvt_pk_bf16_f32 v101, v64, v65
	v_cvt_pk_bf16_f32 v121, v68, v69
	v_pk_mul_f32 v[68:69], v[168:169], v[108:109] op_sel_hi:[0,1]
	s_waitcnt lgkmcnt(1)
	v_mfma_f32_32x32x16_bf16 v[16:31], v[52:55], v[160:163], v[16:31]
	v_add_u32_e32 v52, v221, v211
	ds_read_b128 v[60:63], v52
	global_load_dwordx4 v[52:55], v[72:73], off
	v_cvt_pk_bf16_f32 v102, v68, v69
	v_mul_f32_e64 v68, v168, v84
	v_mul_f32_e64 v69, v168, v85
	v_cvt_pk_bf16_f32 v106, v68, v69
	v_add_u32_e32 v68, v221, v207
	s_waitcnt lgkmcnt(1)
	v_mfma_f32_32x32x16_bf16 v[32:47], v[56:59], v[156:159], v[32:47]
	v_mul_f32_e64 v58, v168, v104
	v_mul_f32_e64 v59, v168, v105
	v_cvt_pk_bf16_f32 v100, v58, v59
	v_add_u32_e32 v58, v221, v212
	ds_read_b128 v[64:67], v58
	v_pk_mul_f32 v[56:57], v[168:169], v[110:111] op_sel_hi:[0,1]
	v_cvt_pk_bf16_f32 v103, v56, v57
	v_add_u32_e32 v56, v221, v213
	s_waitcnt lgkmcnt(1)
	v_mfma_f32_32x32x16_bf16 v[32:47], v[60:63], v[152:155], v[32:47]
	ds_read_b128 v[60:63], v56
	v_cvt_pk_bf16_f32 v107, v70, v71
	ds_read_b128 v[68:71], v68
	v_mul_f32_e64 v76, v168, v76
	v_mul_f32_e64 v77, v168, v77
	v_cvt_pk_bf16_f32 v118, v76, v77
	v_pk_mul_f32 v[74:75], v[168:169], v[92:93] op_sel_hi:[0,1]
	v_pk_mul_f32 v[76:77], v[168:169], v[94:95] op_sel_hi:[0,1]
	s_waitcnt lgkmcnt(2)
	v_mfma_f32_32x32x16_bf16 v[32:47], v[64:67], v[148:151], v[32:47]
	v_mul_f32_e64 v64, v168, v80
	v_mul_f32_e64 v65, v168, v81
	v_mul_f32_e64 v66, v168, v82
	v_mul_f32_e64 v67, v168, v83
	v_cvt_pk_bf16_f32 v104, v64, v65
	v_add_u32_e32 v64, v221, v206
	v_cvt_pk_bf16_f32 v105, v66, v67
	ds_read_b128 v[64:67], v64
	global_load_dwordx4 v[56:59], v[72:73], off offset:80
	s_waitcnt lgkmcnt(2)
	v_mfma_f32_32x32x16_bf16 v[32:47], v[60:63], v[128:131], v[32:47]
	v_cvt_pk_bf16_f32 v110, v74, v75
	v_cvt_pk_bf16_f32 v111, v76, v77
	v_cvt_pk_bf16_f32 v108, v78, v79
	global_load_dwordx4 v[60:63], v[72:73], off offset:64
	global_load_dwordx4 v[164:167], v[72:73], off offset:128
	v_add_u32_e32 v94, v218, v207
	s_movk_i32 s4, 0x180
	s_waitcnt lgkmcnt(0)
	v_mfma_f32_32x32x16_bf16 v[32:47], v[64:67], v[144:147], v[32:47]
	v_mul_f32_e64 v64, v168, v90
	v_mul_f32_e64 v65, v168, v91
	v_cvt_pk_bf16_f32 v109, v64, v65
	v_add_u32_e32 v64, v221, v208
	ds_read_b128 v[64:67], v64
	v_add_u32_e32 v90, v218, v206
	ds_read_b128 v[90:93], v90
	v_or_b32_e32 v202, s6, v203
	v_mfma_f32_32x32x16_bf16 v[32:47], v[68:71], v[140:143], v[32:47]
	v_add_u32_e32 v68, v218, v210
	ds_read_b128 v[74:77], v68
	v_add_u32_e32 v68, v218, v211
	v_add_u32_e32 v69, v221, v209
	ds_read_b128 v[78:81], v68
	ds_read_b128 v[82:85], v69
	v_add_u32_e32 v68, v218, v212
	s_waitcnt lgkmcnt(4)
	v_mfma_f32_32x32x16_bf16 v[32:47], v[64:67], v[132:135], v[32:47]
	global_load_dwordx4 v[64:67], v[72:73], off offset:144
	ds_read_b128 v[68:71], v68
	s_sub_i32 s5, 0, s25
	s_waitcnt lgkmcnt(1)
	v_mfma_f32_32x32x16_bf16 v[32:47], v[82:85], v[136:139], v[32:47]
	ds_read_b128 v[82:85], v94
	v_add_u32_e32 v94, v218, v208
	ds_read_b128 v[160:163], v94
	v_add_u32_e32 v94, v218, v209
	ds_read_b128 v[176:179], v94
	s_nop 6
	v_mul_f32_e32 v36, v168, v36
	v_mfma_f32_32x32x16_bf16 v[16:31], v[74:77], v[156:159], v[16:31]
	v_mul_f32_e32 v74, v168, v37
	s_waitcnt vmcnt(5)
	v_pk_mul_f32 v[74:75], v[74:75], v[48:49] op_sel:[0,1] op_sel_hi:[0,0]
	v_pk_fma_f32 v[76:77], v[36:37], v[48:49], v[74:75] neg_lo:[0,0,1] neg_hi:[0,0,1]
	v_pk_fma_f32 v[48:49], v[36:37], v[48:49], v[74:75] op_sel_hi:[0,1,1]
	v_mul_f32_e32 v36, v168, v39
	v_mul_f32_e32 v48, v168, v38
	v_pk_mul_f32 v[74:75], v[36:37], v[50:51] op_sel:[0,1] op_sel_hi:[0,0]
	global_load_dwordx4 v[36:39], v[72:73], off offset:208
	v_mfma_f32_32x32x16_bf16 v[16:31], v[78:81], v[152:155], v[16:31]
	v_fma_f32 v78, v48, v50, -v74
	v_fma_f32 v79, v49, v51, -v75
	v_fma_f32 v50, v48, v50, v74
	v_fma_f32 v51, v48, v51, v75
	v_mul_f32_e32 v48, v168, v33
	v_mul_f32_e32 v32, v168, v32
	s_waitcnt vmcnt(5)
	v_pk_mul_f32 v[74:75], v[48:49], v[52:53] op_sel:[0,1] op_sel_hi:[0,0]
	v_pk_fma_f32 v[80:81], v[32:33], v[52:53], v[74:75] neg_lo:[0,0,1] neg_hi:[0,0,1]
	v_pk_fma_f32 v[52:53], v[32:33], v[52:53], v[74:75] op_sel_hi:[0,1,1]
	v_mul_f32_e32 v48, v168, v34
	v_mul_f32_e32 v50, v168, v35
	global_load_dwordx4 v[32:35], v[72:73], off offset:192
	s_waitcnt lgkmcnt(3)
	v_mfma_f32_32x32x16_bf16 v[16:31], v[68:71], v[148:151], v[16:31]
	v_mul_f32_e64 v68, v50, v55
	v_mul_f32_e64 v69, v50, v54
	v_fma_f32 v70, v48, v54, -v68
	v_fma_f32 v71, v49, v55, -v69
	v_fma_f32 v54, v48, v54, v68
	v_fma_f32 v55, v48, v55, v69
	v_mul_f32_e32 v48, v168, v45
	v_mul_f32_e32 v44, v168, v44
	v_mul_f32_e32 v40, v168, v40
	v_mov_b32_e32 v158, 0
	v_mfma_f32_32x32x16_bf16 v[16:31], v[86:89], v[128:131], v[16:31]
	v_cvt_pk_bf16_f32 v130, v76, v49
	v_cvt_pk_bf16_f32 v131, v78, v51
	v_cvt_pk_bf16_f32 v128, v80, v53
	v_cvt_pk_bf16_f32 v129, v70, v55
	s_cmp_eq_u32 s99, 0
	s_cselect_b32 s101, 1, 0
	s_cselect_b32 s99, 0, 2
	v_mov_b32_e32 v157, 0xf149f2ca
	s_cbranch_scc0 .Linit_done
	v_mov_b32_e32 v157, 0
